# v26 + pj start: gain pointer from SGPR spill lanes (no vector load of the kernarg pointer + full wait)
# baseline (speedup 1.0000x reference)
; #define LAS __attribute__((address_space(3)))
; __device__ __forceinline__ int opaque_tid() { int t = threadIdx.x; asm volatile("" : "+v"(t)); return t; }
; __device__ __forceinline__ void pj_mfma(const Args& a, LAS unsigned char* lds, int layer) {
;     ...
;     LAS float* gl = (LAS float*)(lds + SEG_OFF + 256);
;     { const int t_ = opaque_tid(); if (t_ < 256) { const int w = t_ >> 6, i = t_ & 63; const float* gp_ = w == 0 ? a.in[I_QGF] : w == 1 ? a.in[I_KGF] : w == 2 ? a.in[I_QGD] : a.in[I_KGD]; gl[t_] = gp_[layer * 64 + i]; } }
;     __syncthreads();
.LBB0_200:
	s_or_b64 exec, exec, s[38:39]
	v_mov_b32_e32 v1, v0
	s_movk_i32 s2, 0x100
	s_waitcnt lgkmcnt(0)
	s_barrier
	s_nop 0
	v_cmp_gt_i32_e32 vcc, s2, v1
	s_and_saveexec_b64 s[4:5], vcc
	s_cbranch_execz .LBB0_202
	v_readfirstlane_b32 s2, v1
	s_nop 0
	s_lshr_b32 s2, s2, 6
	v_readlane_b32 s6, v252, 59
	v_readlane_b32 s7, v252, 60
	s_cmp_eq_u32 s2, 1
	s_cbranch_scc0 .Lpjg_1
	v_readlane_b32 s6, v252, 61
	v_readlane_b32 s7, v252, 62
.Lpjg_1:
	s_cmp_eq_u32 s2, 2
	s_cbranch_scc0 .Lpjg_2
	v_readlane_b32 s6, v252, 63
	v_readlane_b32 s7, v255, 0
.Lpjg_2:
	s_cmp_eq_u32 s2, 3
	s_cbranch_scc0 .Lpjg_3
	v_readlane_b32 s6, v255, 1
	v_readlane_b32 s7, v255, 2
.Lpjg_3:
	s_lshl_b32 s2, s62, 6
	v_and_or_b32 v34, v1, 63, s2
	v_lshl_add_u32 v1, v1, 2, 0
	v_add_u32_e32 v1, 0x21f00, v1
	s_nop 3
	v_lshl_add_u64 v[2:3], v[34:35], 2, s[6:7]
	global_load_dword v2, v[2:3], off
	s_waitcnt vmcnt(0)
	ds_write_b32 v1, v2
